# branch-merge GEMM epilogue: e4m3 staging rows XOR-swizzled like the expert-down epilogue
# baseline (speedup 1.0000x reference)
; #define GAS __attribute__((address_space(1)))
; #define PG8_STAGE(bufoff, gbase, voff) do { _Pragma("unroll") for (int _i = 0; _i < 2; ++_i) \
;         __builtin_amdgcn_global_load_lds((const GAS unsigned*)((const GAS char*)(gbase) + (voff)[_i]), (LAS unsigned*)(lds + (bufoff) + ldsw + _i * 8192), 16, 0, 0); } while (0)
; #define PG8_WAIT_V(n) asm volatile("s_waitcnt vmcnt(" #n ")" ::: "memory")
; #define PG8_BAR __builtin_amdgcn_s_barrier()
; #define PG8_OFFS(u, ao, bo) do { _Pragma("unroll") for (int _i = 0; _i < 2; ++_i) { (bo)[_i] = (unsigned)(sRb[_i] * (u).ldb + sC2[_i]); \
;         _Pragma("unroll") for (int _h = 0; _h < 2; ++_h) { int _r = _h * HALF + sR[_i]; if (GATHER) { _r = (u).gl ? (u).gl[_r] : ((_r < (u).gcnt) ? (u).gidx[_r] : 0); } (ao)[_h][_i] = (unsigned)(_r * (u).lda + sC2[_i]); } } } while (0)
; template <class Epi, class Sched, bool GATHER, bool FP8 = false, bool UNI = false>
; __device__ __forceinline__ void gemm_phase(LAS unsigned char* lds, const Sched& S, const Epi& E) {
;     ...
;     f32x4 acc[2][2][4][2];
; #pragma unroll
;     for (int a = 0; a < 2; ++a)
; #pragma unroll
;         for (int b = 0; b < 2; ++b)
; #pragma unroll
;             for (int m = 0; m < 4; ++m)
; #pragma unroll
;                 for (int n = 0; n < 2; ++n) acc[a][b][m][n] = (f32x4){0.f, 0.f, 0.f, 0.f};
;     i32x8 At[4], B0[2], B1[2];
;     unsigned aoc[2][2], boc[2], aon[2][2], bon[2];
;     PG8_OFFS(cur, aoc, boc);
;     {
;         const GAS char* cA = cur.a; const GAS char* cB = cur.b; const size_t hB = (size_t)(Epi::WIDE ? 32 : HALF) * cur.ldb;
;         PG8_STAGE(PG8_SB(0, 0), cB, boc); PG8_STAGE(PG8_SB(0, 1), cB + hB, boc); PG8_STAGE(PG8_SA(0, 0), cA, aoc[0]); PG8_STAGE(PG8_SA(0, 1), cA, aoc[1]);
;         if (wr == 1) PG8_BAR;
;         PG8_WAIT_V(2); PG8_BAR;
;         PG8_STAGE(PG8_SB(1, 0), cB + 128, boc); PG8_STAGE(PG8_SA(1, 0), cA + 128, aoc[0]); PG8_STAGE(PG8_SB(1, 1), cB + hB + 128, boc);
;         PG8_WAIT_V(6); PG8_BAR;
;     }
;     __device__ __forceinline__ bool operator()(f32x4 (&acc)[2][2][4][2], const Unit& u, int wr, int wc, int fr, int fq, LAS unsigned char* scr) const {
;         const int lane = fq * 16 + fr, rowb = u.row0 + wr * 64, colb = u.col0 + wc * 64;
;         const int lr = lane >> 3, lch = lane & 7;
;         const int wo = lr * 128 + ((lch ^ (lr & 7)) * 16);
.LBB0_1035:
	s_add_u32 s57, s4, 0x6ad00000
	s_addc_u32 s58, s5, 0
	s_add_u32 s59, s4, 0x3a00000
	s_addc_u32 s60, s5, 0
	s_add_u32 s61, s4, 0x3fb00000
	s_addc_u32 s62, s5, 0
	s_add_u32 s14, s4, 0x6bd00000
	v_and_b32_e32 v13, 15, v10
	s_addc_u32 s15, s5, 0
	s_waitcnt vmcnt(0)
	v_bfe_u32 v14, v10, 4, 2
	v_lshlrev_b32_e32 v16, 6, v13
	v_lshlrev_b32_e32 v18, 2, v10
	s_add_i32 s64, s22, 0x18000
	s_and_b32 s21, s6, 3
	s_lshl_b32 s63, s16, 6
	s_lshl_b32 s4, s16, 13
	v_lshl_or_b32 v17, v14, 4, v16
	v_and_b32_e32 v18, 32, v18
	s_add_i32 s65, s64, s7
	s_mov_b64 s[16:17], 0x80
	v_bitop3_b32 v19, v17, s4, v18 bitop3:0xde
	s_lshl_b32 s4, s21, 12
	v_lshl_add_u64 v[8:9], v[8:9], 0, s[16:17]
	s_mov_b32 m0, s65
	s_add_i32 s66, s65, 0x2000
	s_add_i32 s67, s49, 0x8000
	s_add_i32 s68, s49, 0xa000
	v_bitop3_b32 v183, v17, s4, v18 bitop3:0xde
	s_waitcnt vmcnt(2)
	s_barrier
	global_load_lds_dwordx4 v[8:9], off
	v_lshl_add_u64 v[6:7], v[6:7], 0, s[16:17]
	s_mov_b32 m0, s66
	s_add_u32 s4, s28, 0x10080
	global_load_lds_dwordx4 v[6:7], off
	v_lshl_add_u64 v[2:3], v[2:3], 0, s[16:17]
	s_mov_b32 m0, s67
	s_addc_u32 s5, s29, 0
	s_add_i32 s69, s22, 0x1c000
	global_load_lds_dwordx4 v[2:3], off
	v_lshl_add_u64 v[2:3], v[4:5], 0, s[16:17]
	s_mov_b32 m0, s68
	s_add_i32 s70, s69, s7
	global_load_lds_dwordx4 v[2:3], off
	v_lshl_add_u64 v[2:3], s[4:5], 0, v[158:159]
	s_mov_b32 m0, s70
	s_add_i32 s71, s70, 0x2000
	global_load_lds_dwordx4 v[2:3], off
	v_lshl_add_u64 v[2:3], s[4:5], 0, v[138:139]
	s_mov_b32 m0, s71
	s_cmpk_lt_u32 s18, 0x100
	global_load_lds_dwordx4 v[2:3], off
	s_cselect_b64 s[18:19], -1, 0
	s_lshl_b32 s4, s6, 11
	v_bfe_u32 v160, v10, 3, 3
	v_lshrrev_b32_e32 v12, 4, v10
	s_add_i32 s4, s22, s4
	v_and_b32_e32 v3, 7, v10
	v_bitop3_b32 v2, v160, v10, 7 bitop3:0x78
	s_waitcnt vmcnt(6)
	s_add_i32 s4, s4, 0x20000
	v_lshlrev_b32_e32 v4, 4, v2
	v_lshlrev_b32_e32 v2, 3, v3
	v_bitop3_b32 v8, v12, v3, 3 bitop3:0x6c
	v_bitop3_b32 v3, v14, v3, 4 bitop3:0x36
	v_lshlrev_b32_e32 v15, 3, v14
	v_lshl_add_u32 v5, v160, 7, s4
	v_lshl_add_u32 v6, v13, 7, s4
	v_add_u32_e32 v7, s4, v16
	v_bfe_u32 v162, v10, 2, 4
	v_lshlrev_b32_e32 v8, 4, v8
	v_lshlrev_b32_e32 v3, 4, v3
	s_lshl_b32 s72, s21, 6
	v_mov_b32_e32 v161, v159
	v_lshl_add_u32 v184, v162, 6, s4
	v_and_b32_e32 v164, 48, v11
	v_mov_b32_e32 v163, v159
	v_mov_b32_e32 v165, v159
	s_movk_i32 s73, 0x800
	s_mov_b32 s36, 16
	s_mov_b32 s21, 0
	v_mov_b64_e32 v[166:167], 0x200
	v_mov_b64_e32 v[168:169], 0x1ff
	v_add_u32_e32 v185, s22, v19
	v_lshlrev_b32_e32 v170, 1, v2
	v_add_u32_e32 v186, v5, v4
	v_add_u32_e32 v187, v6, v8
	v_add_u32_e32 v188, v6, v3
	v_add_u32_e32 v189, v7, v15
	v_lshrrev_b32_e32 v255, 3, v189
	v_and_b32_e32 v255, 0x30, v255
	v_xor_b32_e32 v189, v189, v255
	v_xor_b32_e32 v255, 32, v189
	v_mov_b32_e32 v133, v158
	s_mov_b32 s37, 0
	s_movk_i32 s38, 0x800
	s_movk_i32 s75, 0x800
	s_mov_b32 s74, 0
	v_mov_b32_e32 v2, v159
	v_mov_b32_e32 v3, v159
	v_mov_b32_e32 v4, v159
	v_mov_b32_e32 v5, v159
	v_mov_b32_e32 v6, v159
	v_mov_b32_e32 v7, v159
	v_mov_b32_e32 v8, v159
	v_mov_b32_e32 v9, v159
	v_mov_b32_e32 v10, v159
	v_mov_b32_e32 v11, v159
	v_mov_b32_e32 v12, v159
	v_mov_b32_e32 v13, v159
	v_mov_b32_e32 v14, v159
	v_mov_b32_e32 v15, v159
	v_mov_b32_e32 v16, v159
	v_mov_b32_e32 v17, v159
	v_mov_b32_e32 v18, v159
	v_mov_b32_e32 v19, v159
	v_mov_b32_e32 v20, v159
	v_mov_b32_e32 v21, v159
	v_mov_b32_e32 v22, v159
	v_mov_b32_e32 v23, v159
	v_mov_b32_e32 v24, v159
	v_mov_b32_e32 v25, v159
	v_mov_b32_e32 v26, v159
	v_mov_b32_e32 v27, v159
	v_mov_b32_e32 v28, v159
	v_mov_b32_e32 v29, v159
	v_mov_b32_e32 v30, v159
	v_mov_b32_e32 v31, v159
	v_mov_b32_e32 v32, v159
	v_mov_b32_e32 v33, v159
	v_mov_b32_e32 v34, v159
	v_mov_b32_e32 v35, v159
	v_mov_b32_e32 v36, v159
	v_mov_b32_e32 v37, v159
	v_mov_b32_e32 v38, v159
	v_mov_b32_e32 v39, v159
	v_mov_b32_e32 v40, v159
	v_mov_b32_e32 v41, v159
	v_mov_b32_e32 v42, v159
	v_mov_b32_e32 v43, v159
	v_mov_b32_e32 v44, v159
	v_mov_b32_e32 v45, v159
	v_mov_b32_e32 v46, v159
	v_mov_b32_e32 v47, v159
	v_mov_b32_e32 v48, v159
	v_mov_b32_e32 v49, v159
	v_mov_b32_e32 v50, v159
	v_mov_b32_e32 v51, v159
	v_mov_b32_e32 v52, v159
	v_mov_b32_e32 v53, v159
	v_mov_b32_e32 v54, v159
	v_mov_b32_e32 v55, v159
	v_mov_b32_e32 v56, v159
	v_mov_b32_e32 v57, v159
	v_mov_b32_e32 v58, v159
	v_mov_b32_e32 v59, v159
	v_mov_b32_e32 v60, v159
	v_mov_b32_e32 v61, v159
	v_mov_b32_e32 v62, v159
	v_mov_b32_e32 v63, v159
	v_mov_b32_e32 v64, v159
	v_mov_b32_e32 v65, v159
	v_mov_b32_e32 v66, v159
	v_mov_b32_e32 v67, v159
	v_mov_b32_e32 v68, v159
	v_mov_b32_e32 v69, v159
	v_mov_b32_e32 v70, v159
	v_mov_b32_e32 v71, v159
	v_mov_b32_e32 v72, v159
	v_mov_b32_e32 v73, v159
	v_mov_b32_e32 v74, v159
	v_mov_b32_e32 v75, v159
	v_mov_b32_e32 v76, v159
	v_mov_b32_e32 v77, v159
	v_mov_b32_e32 v78, v159
	v_mov_b32_e32 v79, v159
	v_mov_b32_e32 v80, v159
	v_mov_b32_e32 v81, v159
	v_mov_b32_e32 v82, v159
	v_mov_b32_e32 v83, v159
	v_mov_b32_e32 v84, v159
	v_mov_b32_e32 v85, v159
	v_mov_b32_e32 v86, v159
	v_mov_b32_e32 v87, v159
	v_mov_b32_e32 v88, v159
	v_mov_b32_e32 v89, v159
	v_mov_b32_e32 v90, v159
	v_mov_b32_e32 v91, v159
	v_mov_b32_e32 v92, v159
	v_mov_b32_e32 v93, v159
	v_mov_b32_e32 v94, v159
	v_mov_b32_e32 v95, v159
	v_mov_b32_e32 v96, v159
	v_mov_b32_e32 v97, v159
	v_mov_b32_e32 v102, v159
	v_mov_b32_e32 v103, v159
	v_mov_b32_e32 v104, v159
	v_mov_b32_e32 v105, v159
	v_mov_b32_e32 v110, v159
	v_mov_b32_e32 v111, v159
	v_mov_b32_e32 v112, v159
	v_mov_b32_e32 v113, v159
	v_mov_b32_e32 v98, v159
	v_mov_b32_e32 v99, v159
	v_mov_b32_e32 v100, v159
	v_mov_b32_e32 v101, v159
	v_mov_b32_e32 v106, v159
	v_mov_b32_e32 v107, v159
	v_mov_b32_e32 v108, v159
	v_mov_b32_e32 v109, v159
	v_mov_b32_e32 v114, v159
	v_mov_b32_e32 v115, v159
	v_mov_b32_e32 v116, v159
	v_mov_b32_e32 v117, v159
	v_mov_b32_e32 v118, v159
	v_mov_b32_e32 v119, v159
	v_mov_b32_e32 v120, v159
	v_mov_b32_e32 v121, v159
	v_mov_b32_e32 v122, v159
	v_mov_b32_e32 v123, v159
	v_mov_b32_e32 v124, v159
	v_mov_b32_e32 v125, v159
	v_mov_b32_e32 v126, v159
	v_mov_b32_e32 v127, v159
	v_mov_b32_e32 v128, v159
	v_mov_b32_e32 v129, v159
	s_barrier
	s_branch .LBB0_1038

; #define LAS __attribute__((address_space(3)))
; __device__ __forceinline__ float fdiv(float a, float b) { return a * __builtin_amdgcn_rcpf(b); }
;     __device__ __forceinline__ bool operator()(f32x4 (&acc)[2][2][4][2], const Unit& u, int wr, int wc, int fr, int fq, LAS unsigned char* scr) const {
;     ...
;                 for (int bj = 0; bj < 2; ++bj) { const u32x4 ga = gaf[bj];
;                     float a[8] = {bflo(ga.x), bfhi(ga.x), bflo(ga.y), bfhi(ga.y), bflo(ga.z), bfhi(ga.z), bflo(ga.w), bfhi(ga.w)};
;                     if (seg0) { const u32x4 gh = ghf[bj];
;                         float h[8] = {bflo(gh.x), bfhi(gh.x), bflo(gh.y), bfhi(gh.y), bflo(gh.z), bfhi(gh.z), bflo(gh.w), bfhi(gh.w)};
; #pragma unroll
;                         for (int j = 0; j < 4; ++j) { acc[ai][bj][m][0][j] *= fdiv(h[j], a[j]); acc[ai][bj][m][1][j] *= fdiv(h[4 + j], a[4 + j]); }
;                     } else {
;                         f32x4 v0 = acc[ai][bj][m][0], v1 = acc[ai][bj][m][1];
; #pragma unroll
;                         for (int j = 0; j < 4; ++j) { v0[j] *= a[j]; v1[j] *= a[4 + j]; }
;                         u32x2 w8; int q = __builtin_amdgcn_cvt_pk_fp8_f32(v0[0], v0[1], 0, false); q = __builtin_amdgcn_cvt_pk_fp8_f32(v0[2], v0[3], q, true); w8.x = (unsigned)q;
;                         q = __builtin_amdgcn_cvt_pk_fp8_f32(v1[0], v1[1], 0, false); q = __builtin_amdgcn_cvt_pk_fp8_f32(v1[2], v1[3], q, true); w8.y = (unsigned)q;
;                         *(LAS u32x2*)(scr + fr * 64 + bj * 32 + fq * 8) = w8; } }
;                 if (!seg0) {
;                     const int r = lane >> 2, ch = lane & 3; const u32x4 o = *(const LAS u32x4*)(scr + r * 64 + ch * 16);
.LBB0_1058:
	s_waitcnt lgkmcnt(0)
	v_lshlrev_b32_e32 v145, 16, v138
	v_and_b32_e32 v144, 0xffff0000, v138
	v_lshlrev_b32_e32 v146, 16, v140
	v_and_b32_e32 v143, 0xffff0000, v140
	v_lshlrev_b32_e32 v140, 16, v141
	v_and_b32_e32 v138, 0xffff0000, v141
	v_cndmask_b32_e64 v141, 0, 1, s[38:39]
	v_lshlrev_b32_e32 v142, 16, v139
	v_and_b32_e32 v139, 0xffff0000, v139
	v_cmp_ne_u32_e64 s[6:7], 1, v141
	s_andn2_b64 vcc, exec, s[38:39]
	s_mov_b64 s[38:39], -1
	s_cbranch_vccnz .LBB0_1146
	v_mul_f32_e32 v141, v70, v145
	v_mul_f32_e32 v149, v71, v144
	v_mov_b32_e32 v148, v159
	v_mul_f32_e32 v147, v66, v146
	v_mul_f32_e32 v150, v67, v143
	v_cvt_pk_fp8_f32 v148, v141, v149
	v_mov_b32_e32 v149, v159
	v_cvt_pk_fp8_f32 v149, v147, v150
	v_mul_f32_e32 v151, v72, v142
	v_mul_f32_e32 v152, v68, v140
	v_mul_f32_e32 v141, v73, v139
	v_mul_f32_e32 v147, v69, v138
	v_cvt_pk_fp8_f32 v148, v151, v141 op_sel:[0,0,1]
	v_cvt_pk_fp8_f32 v149, v152, v147 op_sel:[0,0,1]
	ds_write_b64 v255, v[148:149]
	s_cbranch_execz .LBB0_1147
.LBB0_1060:
	s_ashr_i32 s29, s28, 31
	s_and_b64 vcc, exec, s[6:7]
	v_add_u32_e32 v158, v184, v164
	v_lshrrev_b32_e32 v138, 3, v158
	v_and_b32_e32 v138, 0x30, v138
	v_xor_b32_e32 v158, v158, v138
	s_cbranch_vccnz .LBB0_1062

; #define LAS __attribute__((address_space(3)))
; __device__ __forceinline__ float fdiv(float a, float b) { return a * __builtin_amdgcn_rcpf(b); }
;     __device__ __forceinline__ bool operator()(f32x4 (&acc)[2][2][4][2], const Unit& u, int wr, int wc, int fr, int fq, LAS unsigned char* scr) const {
;     ...
;                 for (int bj = 0; bj < 2; ++bj) { const u32x4 ga = gaf[bj];
;                     float a[8] = {bflo(ga.x), bfhi(ga.x), bflo(ga.y), bfhi(ga.y), bflo(ga.z), bfhi(ga.z), bflo(ga.w), bfhi(ga.w)};
;                     if (seg0) { const u32x4 gh = ghf[bj];
;                         float h[8] = {bflo(gh.x), bfhi(gh.x), bflo(gh.y), bfhi(gh.y), bflo(gh.z), bfhi(gh.z), bflo(gh.w), bfhi(gh.w)};
; #pragma unroll
;                         for (int j = 0; j < 4; ++j) { acc[ai][bj][m][0][j] *= fdiv(h[j], a[j]); acc[ai][bj][m][1][j] *= fdiv(h[4 + j], a[4 + j]); }
;                     } else {
;                         f32x4 v0 = acc[ai][bj][m][0], v1 = acc[ai][bj][m][1];
; #pragma unroll
;                         for (int j = 0; j < 4; ++j) { v0[j] *= a[j]; v1[j] *= a[4 + j]; }
;                         u32x2 w8; int q = __builtin_amdgcn_cvt_pk_fp8_f32(v0[0], v0[1], 0, false); q = __builtin_amdgcn_cvt_pk_fp8_f32(v0[2], v0[3], q, true); w8.x = (unsigned)q;
;                         q = __builtin_amdgcn_cvt_pk_fp8_f32(v1[0], v1[1], 0, false); q = __builtin_amdgcn_cvt_pk_fp8_f32(v1[2], v1[3], q, true); w8.y = (unsigned)q;
;                         *(LAS u32x2*)(scr + fr * 64 + bj * 32 + fq * 8) = w8; } }
.LBB0_1070:
	s_waitcnt lgkmcnt(0)
	v_lshlrev_b32_e32 v145, 16, v138
	v_and_b32_e32 v144, 0xffff0000, v138
	v_lshlrev_b32_e32 v142, 16, v139
	v_and_b32_e32 v139, 0xffff0000, v139
	v_lshlrev_b32_e32 v146, 16, v140
	v_and_b32_e32 v143, 0xffff0000, v140
	v_lshlrev_b32_e32 v140, 16, v141
	v_and_b32_e32 v138, 0xffff0000, v141
	s_and_b64 vcc, exec, s[6:7]
	s_mov_b64 s[40:41], -1
	s_cbranch_vccnz .LBB0_1148
	v_mul_f32_e32 v141, v62, v145
	v_mul_f32_e32 v149, v63, v144
	v_mov_b32_e32 v148, v159
	v_mul_f32_e32 v147, v58, v146
	v_mul_f32_e32 v150, v59, v143
	v_cvt_pk_fp8_f32 v148, v141, v149
	v_mov_b32_e32 v149, v159
	v_cvt_pk_fp8_f32 v149, v147, v150
	v_mul_f32_e32 v151, v64, v142
	v_mul_f32_e32 v152, v60, v140
	v_mul_f32_e32 v141, v65, v139
	v_mul_f32_e32 v147, v61, v138
	v_cvt_pk_fp8_f32 v148, v151, v141 op_sel:[0,0,1]
	v_cvt_pk_fp8_f32 v149, v152, v147 op_sel:[0,0,1]
	ds_write_b64 v255, v[148:149]
	s_cbranch_execz .LBB0_1149

; #define LAS __attribute__((address_space(3)))
; __device__ __forceinline__ float fdiv(float a, float b) { return a * __builtin_amdgcn_rcpf(b); }
;     __device__ __forceinline__ bool operator()(f32x4 (&acc)[2][2][4][2], const Unit& u, int wr, int wc, int fr, int fq, LAS unsigned char* scr) const {
;     ...
;                 for (int bj = 0; bj < 2; ++bj) { const u32x4 ga = gaf[bj];
;                     float a[8] = {bflo(ga.x), bfhi(ga.x), bflo(ga.y), bfhi(ga.y), bflo(ga.z), bfhi(ga.z), bflo(ga.w), bfhi(ga.w)};
;                     if (seg0) { const u32x4 gh = ghf[bj];
;                         float h[8] = {bflo(gh.x), bfhi(gh.x), bflo(gh.y), bfhi(gh.y), bflo(gh.z), bfhi(gh.z), bflo(gh.w), bfhi(gh.w)};
; #pragma unroll
;                         for (int j = 0; j < 4; ++j) { acc[ai][bj][m][0][j] *= fdiv(h[j], a[j]); acc[ai][bj][m][1][j] *= fdiv(h[4 + j], a[4 + j]); }
;                     } else {
;                         f32x4 v0 = acc[ai][bj][m][0], v1 = acc[ai][bj][m][1];
; #pragma unroll
;                         for (int j = 0; j < 4; ++j) { v0[j] *= a[j]; v1[j] *= a[4 + j]; }
;                         u32x2 w8; int q = __builtin_amdgcn_cvt_pk_fp8_f32(v0[0], v0[1], 0, false); q = __builtin_amdgcn_cvt_pk_fp8_f32(v0[2], v0[3], q, true); w8.x = (unsigned)q;
;                         q = __builtin_amdgcn_cvt_pk_fp8_f32(v1[0], v1[1], 0, false); q = __builtin_amdgcn_cvt_pk_fp8_f32(v1[2], v1[3], q, true); w8.y = (unsigned)q;
;                         *(LAS u32x2*)(scr + fr * 64 + bj * 32 + fq * 8) = w8; } }
.LBB0_1082:
	s_waitcnt lgkmcnt(0)
	v_lshlrev_b32_e32 v145, 16, v138
	v_and_b32_e32 v144, 0xffff0000, v138
	v_lshlrev_b32_e32 v142, 16, v139
	v_and_b32_e32 v139, 0xffff0000, v139
	v_lshlrev_b32_e32 v146, 16, v140
	v_and_b32_e32 v143, 0xffff0000, v140
	v_lshlrev_b32_e32 v140, 16, v141
	v_and_b32_e32 v138, 0xffff0000, v141
	s_and_b64 vcc, exec, s[6:7]
	s_mov_b64 s[40:41], -1
	s_cbranch_vccnz .LBB0_1150
	v_mul_f32_e32 v141, v54, v145
	v_mul_f32_e32 v149, v55, v144
	v_mov_b32_e32 v148, v159
	v_mul_f32_e32 v147, v50, v146
	v_mul_f32_e32 v150, v51, v143
	v_cvt_pk_fp8_f32 v148, v141, v149
	v_mov_b32_e32 v149, v159
	v_cvt_pk_fp8_f32 v149, v147, v150
	v_mul_f32_e32 v151, v56, v142
	v_mul_f32_e32 v152, v52, v140
	v_mul_f32_e32 v141, v57, v139
	v_mul_f32_e32 v147, v53, v138
	v_cvt_pk_fp8_f32 v148, v151, v141 op_sel:[0,0,1]
	v_cvt_pk_fp8_f32 v149, v152, v147 op_sel:[0,0,1]
	ds_write_b64 v255, v[148:149]
	s_cbranch_execz .LBB0_1151

; #define LAS __attribute__((address_space(3)))
; __device__ __forceinline__ float fdiv(float a, float b) { return a * __builtin_amdgcn_rcpf(b); }
;     __device__ __forceinline__ bool operator()(f32x4 (&acc)[2][2][4][2], const Unit& u, int wr, int wc, int fr, int fq, LAS unsigned char* scr) const {
;     ...
;                 for (int bj = 0; bj < 2; ++bj) { const u32x4 ga = gaf[bj];
;                     float a[8] = {bflo(ga.x), bfhi(ga.x), bflo(ga.y), bfhi(ga.y), bflo(ga.z), bfhi(ga.z), bflo(ga.w), bfhi(ga.w)};
;                     if (seg0) { const u32x4 gh = ghf[bj];
;                         float h[8] = {bflo(gh.x), bfhi(gh.x), bflo(gh.y), bfhi(gh.y), bflo(gh.z), bfhi(gh.z), bflo(gh.w), bfhi(gh.w)};
; #pragma unroll
;                         for (int j = 0; j < 4; ++j) { acc[ai][bj][m][0][j] *= fdiv(h[j], a[j]); acc[ai][bj][m][1][j] *= fdiv(h[4 + j], a[4 + j]); }
;                     } else {
;                         f32x4 v0 = acc[ai][bj][m][0], v1 = acc[ai][bj][m][1];
; #pragma unroll
;                         for (int j = 0; j < 4; ++j) { v0[j] *= a[j]; v1[j] *= a[4 + j]; }
;                         u32x2 w8; int q = __builtin_amdgcn_cvt_pk_fp8_f32(v0[0], v0[1], 0, false); q = __builtin_amdgcn_cvt_pk_fp8_f32(v0[2], v0[3], q, true); w8.x = (unsigned)q;
;                         q = __builtin_amdgcn_cvt_pk_fp8_f32(v1[0], v1[1], 0, false); q = __builtin_amdgcn_cvt_pk_fp8_f32(v1[2], v1[3], q, true); w8.y = (unsigned)q;
;                         *(LAS u32x2*)(scr + fr * 64 + bj * 32 + fq * 8) = w8; } }
.LBB0_1094:
	s_waitcnt lgkmcnt(0)
	v_lshlrev_b32_e32 v145, 16, v138
	v_and_b32_e32 v144, 0xffff0000, v138
	v_lshlrev_b32_e32 v142, 16, v139
	v_and_b32_e32 v139, 0xffff0000, v139
	v_lshlrev_b32_e32 v146, 16, v140
	v_and_b32_e32 v143, 0xffff0000, v140
	v_lshlrev_b32_e32 v140, 16, v141
	v_and_b32_e32 v138, 0xffff0000, v141
	s_and_b64 vcc, exec, s[6:7]
	s_mov_b64 s[40:41], -1
	s_cbranch_vccnz .LBB0_1152
	v_mul_f32_e32 v141, v46, v145
	v_mul_f32_e32 v149, v47, v144
	v_mov_b32_e32 v148, v159
	v_mul_f32_e32 v147, v42, v146
	v_mul_f32_e32 v150, v43, v143
	v_cvt_pk_fp8_f32 v148, v141, v149
	v_mov_b32_e32 v149, v159
	v_cvt_pk_fp8_f32 v149, v147, v150
	v_mul_f32_e32 v151, v48, v142
	v_mul_f32_e32 v152, v44, v140
	v_mul_f32_e32 v141, v49, v139
	v_mul_f32_e32 v147, v45, v138
	v_cvt_pk_fp8_f32 v148, v151, v141 op_sel:[0,0,1]
	v_cvt_pk_fp8_f32 v149, v152, v147 op_sel:[0,0,1]
	ds_write_b64 v255, v[148:149]
	s_cbranch_execz .LBB0_1153

; #define LAS __attribute__((address_space(3)))
; __device__ __forceinline__ float fdiv(float a, float b) { return a * __builtin_amdgcn_rcpf(b); }
;     __device__ __forceinline__ bool operator()(f32x4 (&acc)[2][2][4][2], const Unit& u, int wr, int wc, int fr, int fq, LAS unsigned char* scr) const {
;     ...
;                 for (int bj = 0; bj < 2; ++bj) { const u32x4 ga = gaf[bj];
;                     float a[8] = {bflo(ga.x), bfhi(ga.x), bflo(ga.y), bfhi(ga.y), bflo(ga.z), bfhi(ga.z), bflo(ga.w), bfhi(ga.w)};
;                     if (seg0) { const u32x4 gh = ghf[bj];
;                         float h[8] = {bflo(gh.x), bfhi(gh.x), bflo(gh.y), bfhi(gh.y), bflo(gh.z), bfhi(gh.z), bflo(gh.w), bfhi(gh.w)};
; #pragma unroll
;                         for (int j = 0; j < 4; ++j) { acc[ai][bj][m][0][j] *= fdiv(h[j], a[j]); acc[ai][bj][m][1][j] *= fdiv(h[4 + j], a[4 + j]); }
;                     } else {
;                         f32x4 v0 = acc[ai][bj][m][0], v1 = acc[ai][bj][m][1];
; #pragma unroll
;                         for (int j = 0; j < 4; ++j) { v0[j] *= a[j]; v1[j] *= a[4 + j]; }
;                         u32x2 w8; int q = __builtin_amdgcn_cvt_pk_fp8_f32(v0[0], v0[1], 0, false); q = __builtin_amdgcn_cvt_pk_fp8_f32(v0[2], v0[3], q, true); w8.x = (unsigned)q;
;                         q = __builtin_amdgcn_cvt_pk_fp8_f32(v1[0], v1[1], 0, false); q = __builtin_amdgcn_cvt_pk_fp8_f32(v1[2], v1[3], q, true); w8.y = (unsigned)q;
;                         *(LAS u32x2*)(scr + fr * 64 + bj * 32 + fq * 8) = w8; } }
.LBB0_1106:
	s_waitcnt lgkmcnt(0)
	v_lshlrev_b32_e32 v145, 16, v138
	v_and_b32_e32 v144, 0xffff0000, v138
	v_lshlrev_b32_e32 v142, 16, v139
	v_and_b32_e32 v139, 0xffff0000, v139
	v_lshlrev_b32_e32 v146, 16, v140
	v_and_b32_e32 v143, 0xffff0000, v140
	v_lshlrev_b32_e32 v140, 16, v141
	v_and_b32_e32 v138, 0xffff0000, v141
	s_and_b64 vcc, exec, s[6:7]
	s_mov_b64 s[40:41], -1
	s_cbranch_vccnz .LBB0_1154
	v_mul_f32_e32 v141, v6, v145
	v_mul_f32_e32 v149, v7, v144
	v_mov_b32_e32 v148, v159
	v_mul_f32_e32 v147, v2, v146
	v_mul_f32_e32 v150, v3, v143
	v_cvt_pk_fp8_f32 v148, v141, v149
	v_mov_b32_e32 v149, v159
	v_cvt_pk_fp8_f32 v149, v147, v150
	v_mul_f32_e32 v151, v8, v142
	v_mul_f32_e32 v152, v4, v140
	v_mul_f32_e32 v141, v9, v139
	v_mul_f32_e32 v147, v5, v138
	v_cvt_pk_fp8_f32 v148, v151, v141 op_sel:[0,0,1]
	v_cvt_pk_fp8_f32 v149, v152, v147 op_sel:[0,0,1]
	ds_write_b64 v255, v[148:149]
	s_cbranch_execz .LBB0_1155

; #define LAS __attribute__((address_space(3)))
; __device__ __forceinline__ float fdiv(float a, float b) { return a * __builtin_amdgcn_rcpf(b); }
;     __device__ __forceinline__ bool operator()(f32x4 (&acc)[2][2][4][2], const Unit& u, int wr, int wc, int fr, int fq, LAS unsigned char* scr) const {
;     ...
;                 for (int bj = 0; bj < 2; ++bj) { const u32x4 ga = gaf[bj];
;                     float a[8] = {bflo(ga.x), bfhi(ga.x), bflo(ga.y), bfhi(ga.y), bflo(ga.z), bfhi(ga.z), bflo(ga.w), bfhi(ga.w)};
;                     if (seg0) { const u32x4 gh = ghf[bj];
;                         float h[8] = {bflo(gh.x), bfhi(gh.x), bflo(gh.y), bfhi(gh.y), bflo(gh.z), bfhi(gh.z), bflo(gh.w), bfhi(gh.w)};
; #pragma unroll
;                         for (int j = 0; j < 4; ++j) { acc[ai][bj][m][0][j] *= fdiv(h[j], a[j]); acc[ai][bj][m][1][j] *= fdiv(h[4 + j], a[4 + j]); }
;                     } else {
;                         f32x4 v0 = acc[ai][bj][m][0], v1 = acc[ai][bj][m][1];
; #pragma unroll
;                         for (int j = 0; j < 4; ++j) { v0[j] *= a[j]; v1[j] *= a[4 + j]; }
;                         u32x2 w8; int q = __builtin_amdgcn_cvt_pk_fp8_f32(v0[0], v0[1], 0, false); q = __builtin_amdgcn_cvt_pk_fp8_f32(v0[2], v0[3], q, true); w8.x = (unsigned)q;
;                         q = __builtin_amdgcn_cvt_pk_fp8_f32(v1[0], v1[1], 0, false); q = __builtin_amdgcn_cvt_pk_fp8_f32(v1[2], v1[3], q, true); w8.y = (unsigned)q;
;                         *(LAS u32x2*)(scr + fr * 64 + bj * 32 + fq * 8) = w8; } }
.LBB0_1118:
	s_waitcnt lgkmcnt(0)
	v_lshlrev_b32_e32 v145, 16, v138
	v_and_b32_e32 v144, 0xffff0000, v138
	v_lshlrev_b32_e32 v142, 16, v139
	v_and_b32_e32 v139, 0xffff0000, v139
	v_lshlrev_b32_e32 v146, 16, v140
	v_and_b32_e32 v143, 0xffff0000, v140
	v_lshlrev_b32_e32 v140, 16, v141
	v_and_b32_e32 v138, 0xffff0000, v141
	s_and_b64 vcc, exec, s[6:7]
	s_mov_b64 s[40:41], -1
	s_cbranch_vccnz .LBB0_1156
	v_mul_f32_e32 v141, v98, v145
	v_mul_f32_e32 v149, v99, v144
	v_mov_b32_e32 v148, v159
	v_mul_f32_e32 v147, v106, v146
	v_mul_f32_e32 v150, v107, v143
	v_cvt_pk_fp8_f32 v148, v141, v149
	v_mov_b32_e32 v149, v159
	v_cvt_pk_fp8_f32 v149, v147, v150
	v_mul_f32_e32 v151, v100, v142
	v_mul_f32_e32 v152, v108, v140
	v_mul_f32_e32 v141, v101, v139
	v_mul_f32_e32 v147, v109, v138
	v_cvt_pk_fp8_f32 v148, v151, v141 op_sel:[0,0,1]
	v_cvt_pk_fp8_f32 v149, v152, v147 op_sel:[0,0,1]
	ds_write_b64 v255, v[148:149]
	s_cbranch_execz .LBB0_1157

; #define LAS __attribute__((address_space(3)))
; __device__ __forceinline__ float fdiv(float a, float b) { return a * __builtin_amdgcn_rcpf(b); }
;     __device__ __forceinline__ bool operator()(f32x4 (&acc)[2][2][4][2], const Unit& u, int wr, int wc, int fr, int fq, LAS unsigned char* scr) const {
;     ...
;                 for (int bj = 0; bj < 2; ++bj) { const u32x4 ga = gaf[bj];
;                     float a[8] = {bflo(ga.x), bfhi(ga.x), bflo(ga.y), bfhi(ga.y), bflo(ga.z), bfhi(ga.z), bflo(ga.w), bfhi(ga.w)};
;                     if (seg0) { const u32x4 gh = ghf[bj];
;                         float h[8] = {bflo(gh.x), bfhi(gh.x), bflo(gh.y), bfhi(gh.y), bflo(gh.z), bfhi(gh.z), bflo(gh.w), bfhi(gh.w)};
; #pragma unroll
;                         for (int j = 0; j < 4; ++j) { acc[ai][bj][m][0][j] *= fdiv(h[j], a[j]); acc[ai][bj][m][1][j] *= fdiv(h[4 + j], a[4 + j]); }
;                     } else {
;                         f32x4 v0 = acc[ai][bj][m][0], v1 = acc[ai][bj][m][1];
; #pragma unroll
;                         for (int j = 0; j < 4; ++j) { v0[j] *= a[j]; v1[j] *= a[4 + j]; }
;                         u32x2 w8; int q = __builtin_amdgcn_cvt_pk_fp8_f32(v0[0], v0[1], 0, false); q = __builtin_amdgcn_cvt_pk_fp8_f32(v0[2], v0[3], q, true); w8.x = (unsigned)q;
;                         q = __builtin_amdgcn_cvt_pk_fp8_f32(v1[0], v1[1], 0, false); q = __builtin_amdgcn_cvt_pk_fp8_f32(v1[2], v1[3], q, true); w8.y = (unsigned)q;
;                         *(LAS u32x2*)(scr + fr * 64 + bj * 32 + fq * 8) = w8; } }
.LBB0_1130:
	s_waitcnt lgkmcnt(0)
	v_lshlrev_b32_e32 v145, 16, v138
	v_and_b32_e32 v144, 0xffff0000, v138
	v_lshlrev_b32_e32 v142, 16, v139
	v_and_b32_e32 v139, 0xffff0000, v139
	v_lshlrev_b32_e32 v146, 16, v140
	v_and_b32_e32 v143, 0xffff0000, v140
	v_lshlrev_b32_e32 v140, 16, v141
	v_and_b32_e32 v138, 0xffff0000, v141
	s_and_b64 vcc, exec, s[6:7]
	s_mov_b64 s[40:41], -1
	s_cbranch_vccnz .LBB0_1158
	v_mul_f32_e32 v141, v114, v145
	v_mul_f32_e32 v149, v115, v144
	v_mov_b32_e32 v148, v159
	v_mul_f32_e32 v147, v118, v146
	v_mul_f32_e32 v150, v119, v143
	v_cvt_pk_fp8_f32 v148, v141, v149
	v_mov_b32_e32 v149, v159
	v_cvt_pk_fp8_f32 v149, v147, v150
	v_mul_f32_e32 v151, v116, v142
	v_mul_f32_e32 v152, v120, v140
	v_mul_f32_e32 v141, v117, v139
	v_mul_f32_e32 v147, v121, v138
	v_cvt_pk_fp8_f32 v148, v151, v141 op_sel:[0,0,1]
	v_cvt_pk_fp8_f32 v149, v152, v147 op_sel:[0,0,1]
	ds_write_b64 v255, v[148:149]
	s_cbranch_execz .LBB0_1159

; #define LAS __attribute__((address_space(3)))
; __device__ __forceinline__ float fdiv(float a, float b) { return a * __builtin_amdgcn_rcpf(b); }
;     __device__ __forceinline__ bool operator()(f32x4 (&acc)[2][2][4][2], const Unit& u, int wr, int wc, int fr, int fq, LAS unsigned char* scr) const {
;     ...
;                 for (int bj = 0; bj < 2; ++bj) { const u32x4 ga = gaf[bj];
;                     float a[8] = {bflo(ga.x), bfhi(ga.x), bflo(ga.y), bfhi(ga.y), bflo(ga.z), bfhi(ga.z), bflo(ga.w), bfhi(ga.w)};
;                     if (seg0) { const u32x4 gh = ghf[bj];
;                         float h[8] = {bflo(gh.x), bfhi(gh.x), bflo(gh.y), bfhi(gh.y), bflo(gh.z), bfhi(gh.z), bflo(gh.w), bfhi(gh.w)};
; #pragma unroll
;                         for (int j = 0; j < 4; ++j) { acc[ai][bj][m][0][j] *= fdiv(h[j], a[j]); acc[ai][bj][m][1][j] *= fdiv(h[4 + j], a[4 + j]); }
;                     } else {
;                         f32x4 v0 = acc[ai][bj][m][0], v1 = acc[ai][bj][m][1];
; #pragma unroll
;                         for (int j = 0; j < 4; ++j) { v0[j] *= a[j]; v1[j] *= a[4 + j]; }
;                         u32x2 w8; int q = __builtin_amdgcn_cvt_pk_fp8_f32(v0[0], v0[1], 0, false); q = __builtin_amdgcn_cvt_pk_fp8_f32(v0[2], v0[3], q, true); w8.x = (unsigned)q;
;                         q = __builtin_amdgcn_cvt_pk_fp8_f32(v1[0], v1[1], 0, false); q = __builtin_amdgcn_cvt_pk_fp8_f32(v1[2], v1[3], q, true); w8.y = (unsigned)q;
;                         *(LAS u32x2*)(scr + fr * 64 + bj * 32 + fq * 8) = w8; } }
.LBB0_1142:
	s_waitcnt lgkmcnt(0)
	v_lshlrev_b32_e32 v143, 16, v138
	v_and_b32_e32 v142, 0xffff0000, v138
	v_lshlrev_b32_e32 v136, 16, v139
	v_and_b32_e32 v135, 0xffff0000, v139
	v_lshlrev_b32_e32 v139, 16, v140
	v_and_b32_e32 v138, 0xffff0000, v140
	v_lshlrev_b32_e32 v137, 16, v141
	v_and_b32_e32 v134, 0xffff0000, v141
	s_and_b64 vcc, exec, s[6:7]
	s_mov_b64 s[8:9], -1
	s_cbranch_vccnz .LBB0_1160
	v_mul_f32_e32 v141, v122, v143
	v_mul_f32_e32 v145, v123, v142
	v_mov_b32_e32 v140, v159
	v_mul_f32_e32 v144, v126, v139
	v_mul_f32_e32 v146, v127, v138
	v_cvt_pk_fp8_f32 v140, v141, v145
	v_mov_b32_e32 v141, v159
	v_cvt_pk_fp8_f32 v141, v144, v146
	v_mul_f32_e32 v147, v124, v136
	v_mul_f32_e32 v148, v128, v137
	v_mul_f32_e32 v144, v125, v135
	v_mul_f32_e32 v145, v129, v134
	v_cvt_pk_fp8_f32 v140, v147, v144 op_sel:[0,0,1]
	v_cvt_pk_fp8_f32 v141, v148, v145 op_sel:[0,0,1]
	ds_write_b64 v255, v[140:141]
	s_cbranch_execz .LBB0_1161

; #define LAS __attribute__((address_space(3)))
; __device__ __forceinline__ float fdiv(float a, float b) { return a * __builtin_amdgcn_rcpf(b); }
;     __device__ __forceinline__ bool operator()(f32x4 (&acc)[2][2][4][2], const Unit& u, int wr, int wc, int fr, int fq, LAS unsigned char* scr) const {
;     ...
;                     if (seg0) { const u32x4 gh = ghf[bj];
;                         float h[8] = {bflo(gh.x), bfhi(gh.x), bflo(gh.y), bfhi(gh.y), bflo(gh.z), bfhi(gh.z), bflo(gh.w), bfhi(gh.w)};
; #pragma unroll
;                         for (int j = 0; j < 4; ++j) { acc[ai][bj][m][0][j] *= fdiv(h[j], a[j]); acc[ai][bj][m][1][j] *= fdiv(h[4 + j], a[4 + j]); }
;     ...
;                 if (!seg0) {
;                     const int r = lane >> 2, ch = lane & 3; const u32x4 o = *(const LAS u32x4*)(scr + r * 64 + ch * 16);
.LBB0_1147:
	v_rcp_f32_e32 v148, v145
	v_rcp_f32_e32 v149, v144
	v_rcp_f32_e32 v144, v146
	v_rcp_f32_e32 v145, v143
	v_lshlrev_b32_e32 v146, 16, v130
	v_and_b32_e32 v147, 0xffff0000, v130
	v_pk_mul_f32 v[146:147], v[148:149], v[146:147]
	v_rcp_f32_e32 v142, v142
	v_rcp_f32_e32 v143, v139
	v_rcp_f32_e32 v140, v140
	v_rcp_f32_e32 v141, v138
	v_pk_mul_f32 v[70:71], v[70:71], v[146:147]
	v_lshlrev_b32_e32 v146, 16, v132
	v_and_b32_e32 v147, 0xffff0000, v132
	v_pk_mul_f32 v[144:145], v[144:145], v[146:147]
	v_lshlrev_b32_e32 v138, 16, v133
	v_pk_mul_f32 v[66:67], v[66:67], v[144:145]
	v_lshlrev_b32_e32 v144, 16, v131
	v_and_b32_e32 v145, 0xffff0000, v131
	v_and_b32_e32 v139, 0xffff0000, v133
	v_pk_mul_f32 v[142:143], v[142:143], v[144:145]
	v_pk_mul_f32 v[138:139], v[140:141], v[138:139]
	v_pk_mul_f32 v[72:73], v[72:73], v[142:143]
	v_pk_mul_f32 v[68:69], v[68:69], v[138:139]
	s_ashr_i32 s29, s28, 31
	s_and_b64 vcc, exec, s[6:7]
	v_add_u32_e32 v158, v184, v164
	v_lshrrev_b32_e32 v138, 3, v158
	v_and_b32_e32 v138, 0x30, v138
	v_xor_b32_e32 v158, v158, v138
	s_cbranch_vccz .LBB0_1061
	s_branch .LBB0_1062

; #define GAS __attribute__((address_space(1)))
; #define PG8_STAGE(bufoff, gbase, voff) do { _Pragma("unroll") for (int _i = 0; _i < 2; ++_i) \
;         __builtin_amdgcn_global_load_lds((const GAS unsigned*)((const GAS char*)(gbase) + (voff)[_i]), (LAS unsigned*)(lds + (bufoff) + ldsw + _i * 8192), 16, 0, 0); } while (0)
; #define PG8_WAIT_V(n) asm volatile("s_waitcnt vmcnt(" #n ")" ::: "memory")
; #define PG8_BAR __builtin_amdgcn_s_barrier()
; #define PG8_OFFS(u, ao, bo) do { _Pragma("unroll") for (int _i = 0; _i < 2; ++_i) { (bo)[_i] = (unsigned)(sRb[_i] * (u).ldb + sC2[_i]); \
;         _Pragma("unroll") for (int _h = 0; _h < 2; ++_h) { int _r = _h * HALF + sR[_i]; if (GATHER) { _r = (u).gl ? (u).gl[_r] : ((_r < (u).gcnt) ? (u).gidx[_r] : 0); } (ao)[_h][_i] = (unsigned)(_r * (u).lda + sC2[_i]); } } } while (0)
; template <class Epi, class Sched, bool GATHER, bool FP8 = false, bool UNI = false>
; __device__ __forceinline__ void gemm_phase(LAS unsigned char* lds, const Sched& S, const Epi& E) {
;     ...
;     f32x4 acc[2][2][4][2];
; #pragma unroll
;     for (int a = 0; a < 2; ++a)
; #pragma unroll
;         for (int b = 0; b < 2; ++b)
; #pragma unroll
;             for (int m = 0; m < 4; ++m)
; #pragma unroll
;                 for (int n = 0; n < 2; ++n) acc[a][b][m][n] = (f32x4){0.f, 0.f, 0.f, 0.f};
;     i32x8 At[4], B0[2], B1[2];
;     unsigned aoc[2][2], boc[2], aon[2][2], bon[2];
;     PG8_OFFS(cur, aoc, boc);
;     {
;         const GAS char* cA = cur.a; const GAS char* cB = cur.b; const size_t hB = (size_t)(Epi::WIDE ? 32 : HALF) * cur.ldb;
;         PG8_STAGE(PG8_SB(0, 0), cB, boc); PG8_STAGE(PG8_SB(0, 1), cB + hB, boc); PG8_STAGE(PG8_SA(0, 0), cA, aoc[0]); PG8_STAGE(PG8_SA(0, 1), cA, aoc[1]);
;         if (wr == 1) PG8_BAR;
;         PG8_WAIT_V(2); PG8_BAR;
;         PG8_STAGE(PG8_SB(1, 0), cB + 128, boc); PG8_STAGE(PG8_SA(1, 0), cA + 128, aoc[0]); PG8_STAGE(PG8_SB(1, 1), cB + hB + 128, boc);
;         PG8_WAIT_V(6); PG8_BAR;
;     }
;     __device__ __forceinline__ bool operator()(f32x4 (&acc)[2][2][4][2], const Unit& u, int wr, int wc, int fr, int fq, LAS unsigned char* scr) const {
;         const int lane = fq * 16 + fr, rowb = u.row0 + wr * 64, colb = u.col0 + wc * 64;
;         const int lr = lane >> 3, lch = lane & 7;
;         const int wo = lr * 128 + ((lch ^ (lr & 7)) * 16);
.LBB0_2600:
	s_add_u32 s57, s4, 0x6ad00000
	s_addc_u32 s58, s5, 0
	s_add_u32 s59, s4, 0x3a00000
	s_addc_u32 s60, s5, 0
	s_add_u32 s61, s4, 0x3fb00000
	s_addc_u32 s62, s5, 0
	s_add_u32 s14, s4, 0x6bd00000
	v_and_b32_e32 v13, 15, v10
	s_addc_u32 s15, s5, 0
	v_bfe_u32 v14, v10, 4, 2
	v_lshlrev_b32_e32 v16, 6, v13
	v_lshlrev_b32_e32 v18, 2, v10
	s_add_i32 s64, s22, 0x18000
	s_and_b32 s21, s6, 3
	s_lshl_b32 s63, s16, 6
	s_lshl_b32 s4, s16, 13
	v_lshl_or_b32 v17, v14, 4, v16
	v_and_b32_e32 v18, 32, v18
	s_add_i32 s65, s64, s7
	s_mov_b64 s[16:17], 0x80
	v_bitop3_b32 v19, v17, s4, v18 bitop3:0xde
	s_lshl_b32 s4, s21, 12
	v_lshl_add_u64 v[8:9], v[8:9], 0, s[16:17]
	s_mov_b32 m0, s65
	s_add_i32 s66, s65, 0x2000
	s_add_i32 s67, s49, 0x8000
	s_add_i32 s68, s49, 0xa000
	v_bitop3_b32 v183, v17, s4, v18 bitop3:0xde
	s_waitcnt vmcnt(2)
	s_barrier
	global_load_lds_dwordx4 v[8:9], off
	v_lshl_add_u64 v[6:7], v[6:7], 0, s[16:17]
	s_mov_b32 m0, s66
	s_add_u32 s4, s28, 0x10080
	global_load_lds_dwordx4 v[6:7], off
	v_lshl_add_u64 v[2:3], v[2:3], 0, s[16:17]
	s_mov_b32 m0, s67
	s_addc_u32 s5, s29, 0
	s_add_i32 s69, s22, 0x1c000
	global_load_lds_dwordx4 v[2:3], off
	v_lshl_add_u64 v[2:3], v[4:5], 0, s[16:17]
	s_mov_b32 m0, s68
	s_add_i32 s70, s69, s7
	global_load_lds_dwordx4 v[2:3], off
	v_lshl_add_u64 v[2:3], s[4:5], 0, v[158:159]
	s_mov_b32 m0, s70
	s_add_i32 s71, s70, 0x2000
	global_load_lds_dwordx4 v[2:3], off
	v_lshl_add_u64 v[2:3], s[4:5], 0, v[138:139]
	s_mov_b32 m0, s71
	s_cmpk_lt_u32 s18, 0x100
	global_load_lds_dwordx4 v[2:3], off
	s_cselect_b64 s[18:19], -1, 0
	s_lshl_b32 s4, s6, 11
	v_bfe_u32 v160, v10, 3, 3
	v_lshrrev_b32_e32 v12, 4, v10
	s_add_i32 s4, s22, s4
	v_and_b32_e32 v3, 7, v10
	v_bitop3_b32 v2, v160, v10, 7 bitop3:0x78
	s_waitcnt vmcnt(6)
	s_add_i32 s4, s4, 0x20000
	v_lshlrev_b32_e32 v4, 4, v2
	v_lshlrev_b32_e32 v2, 3, v3
	v_bitop3_b32 v8, v12, v3, 3 bitop3:0x6c
	v_bitop3_b32 v3, v14, v3, 4 bitop3:0x36
	v_lshlrev_b32_e32 v15, 3, v14
	v_lshl_add_u32 v5, v160, 7, s4
	v_lshl_add_u32 v6, v13, 7, s4
	v_add_u32_e32 v7, s4, v16
	v_bfe_u32 v162, v10, 2, 4
	v_lshlrev_b32_e32 v8, 4, v8
	v_lshlrev_b32_e32 v3, 4, v3
	s_lshl_b32 s72, s21, 6
	v_mov_b32_e32 v161, v159
	v_lshl_add_u32 v184, v162, 6, s4
	v_and_b32_e32 v164, 48, v11
	v_mov_b32_e32 v163, v159
	v_mov_b32_e32 v165, v159
	s_movk_i32 s73, 0x800
	s_mov_b32 s36, 16
	s_mov_b32 s21, 0
	v_mov_b64_e32 v[166:167], 0x200
	v_mov_b64_e32 v[168:169], 0x1ff
	v_add_u32_e32 v185, s22, v19
	v_lshlrev_b32_e32 v170, 1, v2
	v_add_u32_e32 v186, v5, v4
	v_add_u32_e32 v187, v6, v8
	v_add_u32_e32 v188, v6, v3
	v_add_u32_e32 v189, v7, v15
	v_lshrrev_b32_e32 v255, 3, v189
	v_and_b32_e32 v255, 0x30, v255
	v_xor_b32_e32 v189, v189, v255
	v_xor_b32_e32 v255, 32, v189
	v_mov_b32_e32 v133, v158
	s_mov_b32 s37, 0
	s_movk_i32 s38, 0x800
	s_movk_i32 s75, 0x800
	s_mov_b32 s74, 0
	v_mov_b32_e32 v2, v159
	v_mov_b32_e32 v3, v159
	v_mov_b32_e32 v4, v159
	v_mov_b32_e32 v5, v159
	v_mov_b32_e32 v6, v159
	v_mov_b32_e32 v7, v159
	v_mov_b32_e32 v8, v159
	v_mov_b32_e32 v9, v159
	v_mov_b32_e32 v10, v159
	v_mov_b32_e32 v11, v159
	v_mov_b32_e32 v12, v159
	v_mov_b32_e32 v13, v159
	v_mov_b32_e32 v14, v159
	v_mov_b32_e32 v15, v159
	v_mov_b32_e32 v16, v159
	v_mov_b32_e32 v17, v159
	v_mov_b32_e32 v18, v159
	v_mov_b32_e32 v19, v159
	v_mov_b32_e32 v20, v159
	v_mov_b32_e32 v21, v159
	v_mov_b32_e32 v22, v159
	v_mov_b32_e32 v23, v159
	v_mov_b32_e32 v24, v159
	v_mov_b32_e32 v25, v159
	v_mov_b32_e32 v26, v159
	v_mov_b32_e32 v27, v159
	v_mov_b32_e32 v28, v159
	v_mov_b32_e32 v29, v159
	v_mov_b32_e32 v30, v159
	v_mov_b32_e32 v31, v159
	v_mov_b32_e32 v32, v159
	v_mov_b32_e32 v33, v159
	v_mov_b32_e32 v34, v159
	v_mov_b32_e32 v35, v159
	v_mov_b32_e32 v36, v159
	v_mov_b32_e32 v37, v159
	v_mov_b32_e32 v38, v159
	v_mov_b32_e32 v39, v159
	v_mov_b32_e32 v40, v159
	v_mov_b32_e32 v41, v159
	v_mov_b32_e32 v42, v159
	v_mov_b32_e32 v43, v159
	v_mov_b32_e32 v44, v159
	v_mov_b32_e32 v45, v159
	v_mov_b32_e32 v46, v159
	v_mov_b32_e32 v47, v159
	v_mov_b32_e32 v48, v159
	v_mov_b32_e32 v49, v159
	v_mov_b32_e32 v50, v159
	v_mov_b32_e32 v51, v159
	v_mov_b32_e32 v52, v159
	v_mov_b32_e32 v53, v159
	v_mov_b32_e32 v54, v159
	v_mov_b32_e32 v55, v159
	v_mov_b32_e32 v56, v159
	v_mov_b32_e32 v57, v159
	v_mov_b32_e32 v58, v159
	v_mov_b32_e32 v59, v159
	v_mov_b32_e32 v60, v159
	v_mov_b32_e32 v61, v159
	v_mov_b32_e32 v62, v159
	v_mov_b32_e32 v63, v159
	v_mov_b32_e32 v64, v159
	v_mov_b32_e32 v65, v159
	v_mov_b32_e32 v66, v159
	v_mov_b32_e32 v67, v159
	v_mov_b32_e32 v68, v159
	v_mov_b32_e32 v69, v159
	v_mov_b32_e32 v70, v159
	v_mov_b32_e32 v71, v159
	v_mov_b32_e32 v72, v159
	v_mov_b32_e32 v73, v159
	v_mov_b32_e32 v74, v159
	v_mov_b32_e32 v75, v159
	v_mov_b32_e32 v76, v159
	v_mov_b32_e32 v77, v159
	v_mov_b32_e32 v78, v159
	v_mov_b32_e32 v79, v159
	v_mov_b32_e32 v80, v159
	v_mov_b32_e32 v81, v159
	v_mov_b32_e32 v82, v159
	v_mov_b32_e32 v83, v159
	v_mov_b32_e32 v84, v159
	v_mov_b32_e32 v85, v159
	v_mov_b32_e32 v86, v159
	v_mov_b32_e32 v87, v159
	v_mov_b32_e32 v88, v159
	v_mov_b32_e32 v89, v159
	v_mov_b32_e32 v90, v159
	v_mov_b32_e32 v91, v159
	v_mov_b32_e32 v92, v159
	v_mov_b32_e32 v93, v159
	v_mov_b32_e32 v94, v159
	v_mov_b32_e32 v95, v159
	v_mov_b32_e32 v96, v159
	v_mov_b32_e32 v97, v159
	v_mov_b32_e32 v102, v159
	v_mov_b32_e32 v103, v159
	v_mov_b32_e32 v104, v159
	v_mov_b32_e32 v105, v159
	v_mov_b32_e32 v110, v159
	v_mov_b32_e32 v111, v159
	v_mov_b32_e32 v112, v159
	v_mov_b32_e32 v113, v159
	v_mov_b32_e32 v98, v159
	v_mov_b32_e32 v99, v159
	v_mov_b32_e32 v100, v159
	v_mov_b32_e32 v101, v159
	v_mov_b32_e32 v106, v159
	v_mov_b32_e32 v107, v159
	v_mov_b32_e32 v108, v159
	v_mov_b32_e32 v109, v159
	v_mov_b32_e32 v114, v159
	v_mov_b32_e32 v115, v159
	v_mov_b32_e32 v116, v159
	v_mov_b32_e32 v117, v159
	v_mov_b32_e32 v118, v159
	v_mov_b32_e32 v119, v159
	v_mov_b32_e32 v120, v159
	v_mov_b32_e32 v121, v159
	v_mov_b32_e32 v122, v159
	v_mov_b32_e32 v123, v159
	v_mov_b32_e32 v124, v159
	v_mov_b32_e32 v125, v159
	v_mov_b32_e32 v126, v159
	v_mov_b32_e32 v127, v159
	v_mov_b32_e32 v128, v159
	v_mov_b32_e32 v129, v159
	s_barrier
	s_branch .LBB0_2603
